# second poll bank delayed by s_sleep 1 (bank offset fine-tune)
# baseline (speedup 1.0000x reference)
.Lr0_rdy:
	v_lshl_add_u32 v66, s54, 11, v1
	ds_read_b128 a[0:3], v66
	ds_read_b128 a[4:7], v66 offset:1024
	s_cmp_eq_u32 s54, 0
	s_cbranch_scc1 .Lr0_first
	s_sleep 1
	global_load_dwordx4 v[164:167], v[196:197], off nt
	global_load_dwordx4 v[168:171], v[196:197], off offset:1024 nt
	global_load_dwordx4 v[172:175], v[196:197], off offset:2048 nt
	global_load_dwordx4 v[176:179], v[196:197], off offset:3072 nt
	global_load_dwordx4 v[180:183], v[198:199], off nt
	global_load_dwordx4 v[184:187], v[198:199], off offset:1024 nt
	global_load_dwordx4 v[188:191], v[198:199], off offset:2048 nt
	global_load_dwordx4 v[192:195], v[198:199], off offset:3072 nt
	s_mov_b32 s55, 0
	s_waitcnt lgkmcnt(0)
